# C3 epilogue: pair adjacent 16-row groups with v_permlane16_swap and store dwordx4 (8 instead of 16 stores per unit and wave)
# speedup vs baseline: 1.0251x; 1.0084x over previous
; #define LAS __attribute__((address_space(3)))
; __device__ __forceinline__ unsigned pk4_fp8(float a, float b, float c, float d) {
;     a = fminf(fmaxf(a, -448.f), 448.f); b = fminf(fmaxf(b, -448.f), 448.f); c = fminf(fmaxf(c, -448.f), 448.f); d = fminf(fmaxf(d, -448.f), 448.f);
;     int r = 0; r = __builtin_amdgcn_cvt_pk_fp8_f32(a, b, r, false); r = __builtin_amdgcn_cvt_pk_fp8_f32(c, d, r, true); return (unsigned)r;
;     __device__ __forceinline__ void operator()(const f32x4 (&acc)[2][2][4][2], const UnitD& u, int wr, int wc, int fr, int fq) const {
;         const int row0 = u.r0 + wr * 64 + fr, col0 = u.c0 + wc * 32 + 8 * fq;
;         const LAS float* bias = bl_lds + u.ui * 256 + wc * 32 + 8 * fq;
; #pragma unroll
;         for (int bj = 0; bj < 2; ++bj) { const f32x4 bv0 = *(const LAS f32x4*)(bias + bj * 128) * QS_YS, bv1 = *(const LAS f32x4*)(bias + bj * 128 + 4) * QS_YS;
; #pragma unroll
;             for (int ai = 0; ai < 2; ++ai)
; #pragma unroll
;                 for (int m = 0; m < 4; ++m) { unsigned char* rowp = Y + (size_t)(row0 + ai * 128 + m * 16) * DM + col0 + bj * 128;
;                     const f32x4 v0 = acc[ai][bj][m][0] * (QS_YS / (QS_ACT * QS_WDOWN)) + bv0, v1 = acc[ai][bj][m][1] * (QS_YS / (QS_ACT * QS_WDOWN)) + bv1;
;                     u32x2 w; w.x = pk4_fp8(v0[0], v0[1], v0[2], v0[3]); w.y = pk4_fp8(v1[0], v1[1], v1[2], v1[3]);
;                     *(u32x2*)rowp = w; } }
.LBB0_872:
	v_bfe_u32 v152, v136, 4, 1
	v_mov_b32_e32 v128, v136
	v_mul_u32_u24_e32 v152, 0x3ff8, v152
	s_mov_b64 s[16:17], 0x4000
	v_and_b32_e32 v129, 15, v128
	v_ashrrev_i32_e32 v134, 2, v128
	v_lshrrev_b32_e32 v128, 1, v128
	v_and_b32_e32 v130, 0x60, v128
	v_and_b32_e32 v128, 24, v128
	v_add3_u32 v148, v130, s14, v128
	s_lshl_b32 s14, s64, 10
	s_add_i32 s14, s14, 0
	s_add_i32 s14, s14, 0x23100
	v_lshlrev_b32_e32 v130, 2, v130
	v_lshlrev_b32_e32 v128, 2, v128
	v_add3_u32 v143, s14, v130, v128
	ds_read_b128 v[130:133], v143
	ds_read_b128 v[144:147], v143 offset:16
	v_and_or_b32 v128, v134, s39, v129
	v_add_u32_e32 v150, s59, v128
	v_ashrrev_i32_e32 v151, 31, v150
	s_waitcnt lgkmcnt(0)
	v_pk_mul_f32 v[130:131], v[130:131], s[80:81] op_sel_hi:[1,0]
	v_pk_mul_f32 v[134:135], v[144:145], s[80:81] op_sel_hi:[1,0]
	v_pk_fma_f32 v[124:125], v[124:125], s[82:83], v[130:131] op_sel_hi:[1,0,1]
	v_pk_fma_f32 v[120:121], v[120:121], s[82:83], v[134:135] op_sel_hi:[1,0,1]
	v_med3_f32 v144, v124, s51, v187
	v_med3_f32 v125, v125, s51, v187
	v_mov_b32_e32 v124, v153
	v_cvt_pk_fp8_f32 v124, v144, v125
	v_med3_f32 v120, v120, s51, v187
	v_med3_f32 v121, v121, s51, v187
	v_mov_b32_e32 v125, v153
	v_cvt_pk_fp8_f32 v125, v120, v121
	v_pk_mul_f32 v[128:129], v[132:133], s[80:81] op_sel_hi:[1,0]
	v_pk_mul_f32 v[132:133], v[146:147], s[80:81] op_sel_hi:[1,0]
	v_pk_fma_f32 v[126:127], v[126:127], s[82:83], v[128:129] op_sel_hi:[1,0,1]
	v_pk_fma_f32 v[122:123], v[122:123], s[82:83], v[132:133] op_sel_hi:[1,0,1]
	v_med3_f32 v126, v126, s51, v187
	v_med3_f32 v127, v127, s51, v187
	v_med3_f32 v120, v122, s51, v187
	v_med3_f32 v121, v123, s51, v187
	v_cvt_pk_fp8_f32 v124, v126, v127 op_sel:[0,0,1]
	v_cvt_pk_fp8_f32 v125, v120, v121 op_sel:[0,0,1]
	v_lshlrev_b64 v[120:121], 10, v[150:151]
	v_ashrrev_i32_e32 v149, 31, v148
	v_lshl_add_u64 v[120:121], s[2:3], 0, v[120:121]
	v_lshl_add_u64 v[120:121], v[120:121], 0, v[148:149]
	v_pk_fma_f32 v[116:117], v[116:117], s[82:83], v[130:131] op_sel_hi:[1,0,1]
	v_mov_b32_e32 v208, v124
	v_mov_b32_e32 v209, v125
	v_pk_fma_f32 v[112:113], v[112:113], s[82:83], v[134:135] op_sel_hi:[1,0,1]
	v_med3_f32 v124, v116, s51, v187
	v_med3_f32 v117, v117, s51, v187
	v_mov_b32_e32 v116, v153
	v_pk_fma_f32 v[114:115], v[114:115], s[82:83], v[132:133] op_sel_hi:[1,0,1]
	v_cvt_pk_fp8_f32 v116, v124, v117
	v_med3_f32 v112, v112, s51, v187
	v_med3_f32 v113, v113, s51, v187
	v_mov_b32_e32 v117, v153
	v_pk_fma_f32 v[108:109], v[108:109], s[82:83], v[130:131] op_sel_hi:[1,0,1]
	v_cvt_pk_fp8_f32 v117, v112, v113
	v_med3_f32 v112, v114, s51, v187
	v_pk_fma_f32 v[104:105], v[104:105], s[82:83], v[134:135] op_sel_hi:[1,0,1]
	v_med3_f32 v114, v108, s51, v187
	v_med3_f32 v109, v109, s51, v187
	v_mov_b32_e32 v108, v153
	v_pk_fma_f32 v[106:107], v[106:107], s[82:83], v[132:133] op_sel_hi:[1,0,1]
	v_cvt_pk_fp8_f32 v108, v114, v109
	v_med3_f32 v104, v104, s51, v187
	v_med3_f32 v105, v105, s51, v187
	v_mov_b32_e32 v109, v153
	v_pk_fma_f32 v[100:101], v[100:101], s[82:83], v[130:131] op_sel_hi:[1,0,1]
	v_cvt_pk_fp8_f32 v109, v104, v105
	v_med3_f32 v104, v106, s51, v187
	v_pk_fma_f32 v[96:97], v[96:97], s[82:83], v[134:135] op_sel_hi:[1,0,1]
	v_med3_f32 v106, v100, s51, v187
	v_med3_f32 v101, v101, s51, v187
	v_mov_b32_e32 v100, v153
	v_pk_fma_f32 v[98:99], v[98:99], s[82:83], v[132:133] op_sel_hi:[1,0,1]
	v_cvt_pk_fp8_f32 v100, v106, v101
	v_med3_f32 v96, v96, s51, v187
	v_med3_f32 v97, v97, s51, v187
	v_mov_b32_e32 v101, v153
	v_pk_fma_f32 v[92:93], v[92:93], s[82:83], v[130:131] op_sel_hi:[1,0,1]
	v_cvt_pk_fp8_f32 v101, v96, v97
	v_med3_f32 v96, v98, s51, v187
	v_pk_fma_f32 v[88:89], v[88:89], s[82:83], v[134:135] op_sel_hi:[1,0,1]
	v_med3_f32 v98, v92, s51, v187
	v_med3_f32 v93, v93, s51, v187
	v_mov_b32_e32 v92, v153
	v_med3_f32 v113, v115, s51, v187
	s_movk_i32 s14, 0x4000
	v_pk_fma_f32 v[90:91], v[90:91], s[82:83], v[132:133] op_sel_hi:[1,0,1]
	v_cvt_pk_fp8_f32 v92, v98, v93
	v_med3_f32 v88, v88, s51, v187
	v_med3_f32 v89, v89, s51, v187
	v_mov_b32_e32 v93, v153
	v_pk_fma_f32 v[84:85], v[84:85], s[82:83], v[130:131] op_sel_hi:[1,0,1]
	v_cvt_pk_fp8_f32 v117, v112, v113 op_sel:[0,0,1]
	v_add_co_u32_e32 v112, vcc, s14, v120
	v_cvt_pk_fp8_f32 v93, v88, v89
	v_med3_f32 v88, v90, s51, v187
	v_pk_fma_f32 v[80:81], v[80:81], s[82:83], v[134:135] op_sel_hi:[1,0,1]
	v_med3_f32 v90, v84, s51, v187
	v_med3_f32 v85, v85, s51, v187
	v_mov_b32_e32 v84, v153
	v_addc_co_u32_e32 v113, vcc, 0, v121, vcc
	v_med3_f32 v105, v107, s51, v187
	s_mov_b32 s14, 0x8000
	v_pk_fma_f32 v[82:83], v[82:83], s[82:83], v[132:133] op_sel_hi:[1,0,1]
	v_cvt_pk_fp8_f32 v84, v90, v85
	v_med3_f32 v80, v80, s51, v187
	v_med3_f32 v81, v81, s51, v187
	v_mov_b32_e32 v85, v153
	v_pk_fma_f32 v[76:77], v[76:77], s[82:83], v[130:131] op_sel_hi:[1,0,1]
	v_cvt_pk_fp8_f32 v109, v104, v105 op_sel:[0,0,1]
	v_add_co_u32_e32 v104, vcc, s14, v120
	v_cvt_pk_fp8_f32 v85, v80, v81
	v_med3_f32 v80, v82, s51, v187
	v_pk_fma_f32 v[72:73], v[72:73], s[82:83], v[134:135] op_sel_hi:[1,0,1]
	v_med3_f32 v82, v76, s51, v187
	v_med3_f32 v77, v77, s51, v187
	v_mov_b32_e32 v76, v153
	v_addc_co_u32_e32 v105, vcc, 0, v121, vcc
	v_med3_f32 v97, v99, s51, v187
	s_mov_b32 s14, 0xc000
	v_cvt_pk_fp8_f32 v76, v82, v77
	v_med3_f32 v72, v72, s51, v187
	v_med3_f32 v73, v73, s51, v187
	v_mov_b32_e32 v77, v153
	v_cvt_pk_fp8_f32 v101, v96, v97 op_sel:[0,0,1]
	v_add_co_u32_e32 v96, vcc, s14, v120
	v_cvt_pk_fp8_f32 v77, v72, v73
	s_nop 0
	v_addc_co_u32_e32 v97, vcc, 0, v121, vcc
	v_med3_f32 v89, v91, s51, v187
	s_mov_b32 s14, 0x20000
	v_pk_fma_f32 v[118:119], v[118:119], s[82:83], v[128:129] op_sel_hi:[1,0,1]
; #define LAS __attribute__((address_space(3)))
; __device__ __forceinline__ unsigned pk4_fp8(float a, float b, float c, float d) {
;     a = fminf(fmaxf(a, -448.f), 448.f); b = fminf(fmaxf(b, -448.f), 448.f); c = fminf(fmaxf(c, -448.f), 448.f); d = fminf(fmaxf(d, -448.f), 448.f);
;     int r = 0; r = __builtin_amdgcn_cvt_pk_fp8_f32(a, b, r, false); r = __builtin_amdgcn_cvt_pk_fp8_f32(c, d, r, true); return (unsigned)r;
;     __device__ __forceinline__ void operator()(const f32x4 (&acc)[2][2][4][2], const UnitD& u, int wr, int wc, int fr, int fq) const {
;         const int row0 = u.r0 + wr * 64 + fr, col0 = u.c0 + wc * 32 + 8 * fq;
;         const LAS float* bias = bl_lds + u.ui * 256 + wc * 32 + 8 * fq;
; #pragma unroll
;         for (int bj = 0; bj < 2; ++bj) { const f32x4 bv0 = *(const LAS f32x4*)(bias + bj * 128) * QS_YS, bv1 = *(const LAS f32x4*)(bias + bj * 128 + 4) * QS_YS;
; #pragma unroll
;             for (int ai = 0; ai < 2; ++ai)
; #pragma unroll
;                 for (int m = 0; m < 4; ++m) { unsigned char* rowp = Y + (size_t)(row0 + ai * 128 + m * 16) * DM + col0 + bj * 128;
;                     const f32x4 v0 = acc[ai][bj][m][0] * (QS_YS / (QS_ACT * QS_WDOWN)) + bv0, v1 = acc[ai][bj][m][1] * (QS_YS / (QS_ACT * QS_WDOWN)) + bv1;
;                     u32x2 w; w.x = pk4_fp8(v0[0], v0[1], v0[2], v0[3]); w.y = pk4_fp8(v1[0], v1[1], v1[2], v1[3]);
;                     *(u32x2*)rowp = w; } }
	v_pk_fma_f32 v[110:111], v[110:111], s[82:83], v[128:129] op_sel_hi:[1,0,1]
	v_pk_fma_f32 v[102:103], v[102:103], s[82:83], v[128:129] op_sel_hi:[1,0,1]
	v_pk_fma_f32 v[94:95], v[94:95], s[82:83], v[128:129] op_sel_hi:[1,0,1]
	v_cvt_pk_fp8_f32 v93, v88, v89 op_sel:[0,0,1]
	v_add_co_u32_e32 v88, vcc, s14, v120
	v_pk_fma_f32 v[86:87], v[86:87], s[82:83], v[128:129] op_sel_hi:[1,0,1]
	v_pk_fma_f32 v[78:79], v[78:79], s[82:83], v[128:129] op_sel_hi:[1,0,1]
	v_pk_fma_f32 v[74:75], v[74:75], s[82:83], v[132:133] op_sel_hi:[1,0,1]
	v_med3_f32 v118, v118, s51, v187
	v_med3_f32 v119, v119, s51, v187
	v_med3_f32 v110, v110, s51, v187
	v_med3_f32 v111, v111, s51, v187
	v_med3_f32 v102, v102, s51, v187
	v_med3_f32 v103, v103, s51, v187
	v_med3_f32 v94, v94, s51, v187
	v_med3_f32 v95, v95, s51, v187
	v_addc_co_u32_e32 v89, vcc, 0, v121, vcc
	v_med3_f32 v86, v86, s51, v187
	v_med3_f32 v87, v87, s51, v187
	v_med3_f32 v81, v83, s51, v187
	s_mov_b32 s14, 0x24000
	v_med3_f32 v78, v78, s51, v187
	v_med3_f32 v79, v79, s51, v187
	v_med3_f32 v72, v74, s51, v187
	v_med3_f32 v73, v75, s51, v187
	v_pk_fma_f32 v[68:69], v[68:69], s[82:83], v[130:131] op_sel_hi:[1,0,1]
	v_pk_fma_f32 v[64:65], v[64:65], s[82:83], v[134:135] op_sel_hi:[1,0,1]
	v_cvt_pk_fp8_f32 v116, v118, v119 op_sel:[0,0,1]
	v_cvt_pk_fp8_f32 v108, v110, v111 op_sel:[0,0,1]
	v_cvt_pk_fp8_f32 v100, v102, v103 op_sel:[0,0,1]
	v_cvt_pk_fp8_f32 v92, v94, v95 op_sel:[0,0,1]
	v_cvt_pk_fp8_f32 v84, v86, v87 op_sel:[0,0,1]
	v_cvt_pk_fp8_f32 v85, v80, v81 op_sel:[0,0,1]
	v_add_co_u32_e32 v80, vcc, s14, v120
	v_cvt_pk_fp8_f32 v76, v78, v79 op_sel:[0,0,1]
	v_cvt_pk_fp8_f32 v77, v72, v73 op_sel:[0,0,1]
	v_med3_f32 v68, v68, s51, v187
	v_med3_f32 v69, v69, s51, v187
	v_mov_b32_e32 v74, v153
	v_med3_f32 v64, v64, s51, v187
	v_med3_f32 v65, v65, s51, v187
	v_mov_b32_e32 v75, v153
	v_addc_co_u32_e32 v81, vcc, 0, v121, vcc
	s_mov_b32 s14, 0x28000
	v_cvt_pk_fp8_f32 v74, v68, v69
	v_cvt_pk_fp8_f32 v75, v64, v65
	v_add_co_u32_e32 v72, vcc, s14, v120
	v_pk_fma_f32 v[70:71], v[70:71], s[82:83], v[128:129] op_sel_hi:[1,0,1]
	s_nop 0
	v_addc_co_u32_e32 v73, vcc, 0, v121, vcc
	v_pk_fma_f32 v[66:67], v[66:67], s[82:83], v[132:133] op_sel_hi:[1,0,1]
	v_mov_b32_e32 v210, v116
	v_mov_b32_e32 v211, v117
	v_mov_b32_e32 v212, v108
	v_mov_b32_e32 v213, v109
	v_mov_b32_e32 v214, v100
	v_mov_b32_e32 v215, v101
	v_mov_b32_e32 v216, v92
	v_mov_b32_e32 v217, v93
	v_mov_b32_e32 v218, v84
	v_mov_b32_e32 v219, v85
	v_mov_b32_e32 v220, v76
	v_mov_b32_e32 v221, v77
	v_permlane16_swap_b32_e32 v208, v210
	v_permlane16_swap_b32_e32 v209, v211
	v_permlane16_swap_b32_e32 v212, v214
	v_permlane16_swap_b32_e32 v213, v215
	v_permlane16_swap_b32_e32 v216, v218
	v_permlane16_swap_b32_e32 v217, v219
	v_lshl_add_u64 v[224:225], v[120:121], 0, v[152:153]
	v_lshl_add_u64 v[226:227], v[104:105], 0, v[152:153]
	v_lshl_add_u64 v[228:229], v[88:89], 0, v[152:153]
	v_lshl_add_u64 v[230:231], v[72:73], 0, v[152:153]
	global_store_dwordx4 v[224:225], v[208:211], off
	global_store_dwordx4 v[226:227], v[212:215], off
	global_store_dwordx4 v[228:229], v[216:219], off
	v_med3_f32 v70, v70, s51, v187
	v_med3_f32 v71, v71, s51, v187
	v_med3_f32 v64, v66, s51, v187
	v_med3_f32 v65, v67, s51, v187
	v_cvt_pk_fp8_f32 v74, v70, v71 op_sel:[0,0,1]
	v_cvt_pk_fp8_f32 v75, v64, v65 op_sel:[0,0,1]
	ds_read_b128 v[64:67], v143 offset:512
	ds_read_b128 v[68:71], v143 offset:528
	s_mov_b32 s14, 0x2c000
	v_add_co_u32_e32 v76, vcc, s14, v120
	s_waitcnt lgkmcnt(0)
	v_pk_mul_f32 v[64:65], v[64:65], s[80:81] op_sel_hi:[1,0]
	v_addc_co_u32_e32 v77, vcc, 0, v121, vcc
	v_pk_mul_f32 v[68:69], v[68:69], s[80:81] op_sel_hi:[1,0]
	v_pk_fma_f32 v[60:61], v[60:61], s[82:83], v[64:65] op_sel_hi:[1,0,1]
	v_mov_b32_e32 v222, v74
	v_mov_b32_e32 v223, v75
	v_pk_fma_f32 v[56:57], v[56:57], s[82:83], v[68:69] op_sel_hi:[1,0,1]
	s_nop 0
	v_permlane16_swap_b32_e32 v220, v222
	v_permlane16_swap_b32_e32 v221, v223
	global_store_dwordx4 v[230:231], v[220:223], off
	v_med3_f32 v74, v60, s51, v187
	v_med3_f32 v61, v61, s51, v187
	v_mov_b32_e32 v60, v153
	v_cvt_pk_fp8_f32 v60, v74, v61
	v_med3_f32 v56, v56, s51, v187
	v_med3_f32 v57, v57, s51, v187
	v_mov_b32_e32 v61, v153
	v_cvt_pk_fp8_f32 v61, v56, v57
	v_pk_mul_f32 v[70:71], v[70:71], s[80:81] op_sel_hi:[1,0]
	v_pk_fma_f32 v[52:53], v[52:53], s[82:83], v[64:65] op_sel_hi:[1,0,1]
	v_pk_fma_f32 v[58:59], v[58:59], s[82:83], v[70:71] op_sel_hi:[1,0,1]
	v_pk_fma_f32 v[48:49], v[48:49], s[82:83], v[68:69] op_sel_hi:[1,0,1]
	v_med3_f32 v56, v58, s51, v187
	v_med3_f32 v57, v59, s51, v187
	v_cvt_pk_fp8_f32 v61, v56, v57 op_sel:[0,0,1]
	v_med3_f32 v56, v52, s51, v187
	v_med3_f32 v53, v53, s51, v187
	v_mov_b32_e32 v52, v153
	v_cvt_pk_fp8_f32 v52, v56, v53
	v_med3_f32 v48, v48, s51, v187
	v_med3_f32 v49, v49, s51, v187
	v_mov_b32_e32 v53, v153
	v_cvt_pk_fp8_f32 v53, v48, v49
	v_pk_fma_f32 v[50:51], v[50:51], s[82:83], v[70:71] op_sel_hi:[1,0,1]
	v_pk_fma_f32 v[44:45], v[44:45], s[82:83], v[64:65] op_sel_hi:[1,0,1]
	v_med3_f32 v48, v50, s51, v187
	v_med3_f32 v49, v51, s51, v187
	v_cvt_pk_fp8_f32 v53, v48, v49 op_sel:[0,0,1]
	v_pk_fma_f32 v[40:41], v[40:41], s[82:83], v[68:69] op_sel_hi:[1,0,1]
	v_med3_f32 v48, v44, s51, v187
	v_med3_f32 v45, v45, s51, v187
	v_mov_b32_e32 v44, v153
	v_cvt_pk_fp8_f32 v44, v48, v45
	v_med3_f32 v40, v40, s51, v187
	v_med3_f32 v41, v41, s51, v187
	v_mov_b32_e32 v45, v153
	v_cvt_pk_fp8_f32 v45, v40, v41
	v_pk_fma_f32 v[42:43], v[42:43], s[82:83], v[70:71] op_sel_hi:[1,0,1]
	v_pk_fma_f32 v[36:37], v[36:37], s[82:83], v[64:65] op_sel_hi:[1,0,1]
	v_med3_f32 v40, v42, s51, v187
	v_med3_f32 v41, v43, s51, v187
	v_cvt_pk_fp8_f32 v45, v40, v41 op_sel:[0,0,1]
; #define LAS __attribute__((address_space(3)))
; __device__ __forceinline__ unsigned pk4_fp8(float a, float b, float c, float d) {
;     a = fminf(fmaxf(a, -448.f), 448.f); b = fminf(fmaxf(b, -448.f), 448.f); c = fminf(fmaxf(c, -448.f), 448.f); d = fminf(fmaxf(d, -448.f), 448.f);
;     int r = 0; r = __builtin_amdgcn_cvt_pk_fp8_f32(a, b, r, false); r = __builtin_amdgcn_cvt_pk_fp8_f32(c, d, r, true); return (unsigned)r;
;     __device__ __forceinline__ void operator()(const f32x4 (&acc)[2][2][4][2], const UnitD& u, int wr, int wc, int fr, int fq) const {
;         const int row0 = u.r0 + wr * 64 + fr, col0 = u.c0 + wc * 32 + 8 * fq;
;         const LAS float* bias = bl_lds + u.ui * 256 + wc * 32 + 8 * fq;
; #pragma unroll
;         for (int bj = 0; bj < 2; ++bj) { const f32x4 bv0 = *(const LAS f32x4*)(bias + bj * 128) * QS_YS, bv1 = *(const LAS f32x4*)(bias + bj * 128 + 4) * QS_YS;
; #pragma unroll
;             for (int ai = 0; ai < 2; ++ai)
; #pragma unroll
;                 for (int m = 0; m < 4; ++m) { unsigned char* rowp = Y + (size_t)(row0 + ai * 128 + m * 16) * DM + col0 + bj * 128;
;                     const f32x4 v0 = acc[ai][bj][m][0] * (QS_YS / (QS_ACT * QS_WDOWN)) + bv0, v1 = acc[ai][bj][m][1] * (QS_YS / (QS_ACT * QS_WDOWN)) + bv1;
;                     u32x2 w; w.x = pk4_fp8(v0[0], v0[1], v0[2], v0[3]); w.y = pk4_fp8(v1[0], v1[1], v1[2], v1[3]);
;                     *(u32x2*)rowp = w; } }
	v_pk_fma_f32 v[32:33], v[32:33], s[82:83], v[68:69] op_sel_hi:[1,0,1]
	v_med3_f32 v40, v36, s51, v187
	v_med3_f32 v37, v37, s51, v187
	v_mov_b32_e32 v36, v153
	v_cvt_pk_fp8_f32 v36, v40, v37
	v_med3_f32 v32, v32, s51, v187
	v_med3_f32 v33, v33, s51, v187
	v_mov_b32_e32 v37, v153
	v_cvt_pk_fp8_f32 v37, v32, v33
	v_pk_fma_f32 v[34:35], v[34:35], s[82:83], v[70:71] op_sel_hi:[1,0,1]
	v_pk_fma_f32 v[28:29], v[28:29], s[82:83], v[64:65] op_sel_hi:[1,0,1]
	v_med3_f32 v32, v34, s51, v187
	v_med3_f32 v33, v35, s51, v187
	v_cvt_pk_fp8_f32 v37, v32, v33 op_sel:[0,0,1]
	v_pk_fma_f32 v[24:25], v[24:25], s[82:83], v[68:69] op_sel_hi:[1,0,1]
	v_med3_f32 v32, v28, s51, v187
	v_med3_f32 v29, v29, s51, v187
	v_mov_b32_e32 v28, v153
	v_cvt_pk_fp8_f32 v28, v32, v29
	v_med3_f32 v24, v24, s51, v187
	v_med3_f32 v25, v25, s51, v187
	v_mov_b32_e32 v29, v153
	v_cvt_pk_fp8_f32 v29, v24, v25
	v_pk_fma_f32 v[26:27], v[26:27], s[82:83], v[70:71] op_sel_hi:[1,0,1]
	v_pk_fma_f32 v[20:21], v[20:21], s[82:83], v[64:65] op_sel_hi:[1,0,1]
	v_med3_f32 v24, v26, s51, v187
	v_med3_f32 v25, v27, s51, v187
	v_cvt_pk_fp8_f32 v29, v24, v25 op_sel:[0,0,1]
	v_pk_fma_f32 v[16:17], v[16:17], s[82:83], v[68:69] op_sel_hi:[1,0,1]
	v_med3_f32 v24, v20, s51, v187
	v_med3_f32 v21, v21, s51, v187
	v_mov_b32_e32 v20, v153
	v_cvt_pk_fp8_f32 v20, v24, v21
	v_med3_f32 v16, v16, s51, v187
	v_med3_f32 v17, v17, s51, v187
	v_mov_b32_e32 v21, v153
	v_cvt_pk_fp8_f32 v21, v16, v17
	v_pk_fma_f32 v[18:19], v[18:19], s[82:83], v[70:71] op_sel_hi:[1,0,1]
	v_pk_fma_f32 v[12:13], v[12:13], s[82:83], v[64:65] op_sel_hi:[1,0,1]
	v_med3_f32 v16, v18, s51, v187
	v_med3_f32 v17, v19, s51, v187
	v_cvt_pk_fp8_f32 v21, v16, v17 op_sel:[0,0,1]
	v_pk_fma_f32 v[8:9], v[8:9], s[82:83], v[68:69] op_sel_hi:[1,0,1]
	v_med3_f32 v16, v12, s51, v187
	v_med3_f32 v13, v13, s51, v187
	v_mov_b32_e32 v12, v153
	v_cvt_pk_fp8_f32 v12, v16, v13
	v_med3_f32 v8, v8, s51, v187
	v_med3_f32 v9, v9, s51, v187
	v_mov_b32_e32 v13, v153
	v_cvt_pk_fp8_f32 v13, v8, v9
	v_pk_fma_f32 v[10:11], v[10:11], s[82:83], v[70:71] op_sel_hi:[1,0,1]
	v_pk_fma_f32 v[4:5], v[4:5], s[82:83], v[64:65] op_sel_hi:[1,0,1]
	v_med3_f32 v8, v10, s51, v187
	v_med3_f32 v9, v11, s51, v187
	v_pk_mul_f32 v[66:67], v[66:67], s[80:81] op_sel_hi:[1,0]
	v_cvt_pk_fp8_f32 v13, v8, v9 op_sel:[0,0,1]
	v_pk_fma_f32 v[0:1], v[0:1], s[82:83], v[68:69] op_sel_hi:[1,0,1]
	v_med3_f32 v8, v4, s51, v187
	v_med3_f32 v5, v5, s51, v187
	v_mov_b32_e32 v4, v153
	v_pk_fma_f32 v[62:63], v[62:63], s[82:83], v[66:67] op_sel_hi:[1,0,1]
	v_pk_fma_f32 v[30:31], v[30:31], s[82:83], v[66:67] op_sel_hi:[1,0,1]
	v_cvt_pk_fp8_f32 v4, v8, v5
	v_med3_f32 v0, v0, s51, v187
	v_med3_f32 v1, v1, s51, v187
	v_mov_b32_e32 v5, v153
	v_lshl_add_u64 v[122:123], v[120:121], 0, s[16:17]
	s_mov_b64 s[16:17], 0xc000
	v_med3_f32 v62, v62, s51, v187
	v_med3_f32 v63, v63, s51, v187
	v_pk_fma_f32 v[54:55], v[54:55], s[82:83], v[66:67] op_sel_hi:[1,0,1]
	v_med3_f32 v30, v30, s51, v187
	v_med3_f32 v31, v31, s51, v187
	v_pk_fma_f32 v[22:23], v[22:23], s[82:83], v[66:67] op_sel_hi:[1,0,1]
	v_cvt_pk_fp8_f32 v5, v0, v1
	v_lshl_add_u64 v[104:105], v[120:121], 0, s[16:17]
	s_mov_b64 s[16:17], 0x20000
	v_cvt_pk_fp8_f32 v60, v62, v63 op_sel:[0,0,1]
	v_med3_f32 v54, v54, s51, v187
	v_med3_f32 v55, v55, s51, v187
	v_pk_fma_f32 v[46:47], v[46:47], s[82:83], v[66:67] op_sel_hi:[1,0,1]
	v_cvt_pk_fp8_f32 v28, v30, v31 op_sel:[0,0,1]
	v_med3_f32 v22, v22, s51, v187
	v_med3_f32 v23, v23, s51, v187
	v_pk_fma_f32 v[14:15], v[14:15], s[82:83], v[66:67] op_sel_hi:[1,0,1]
	v_lshl_add_u64 v[96:97], v[120:121], 0, s[16:17]
	s_mov_b64 s[16:17], 0x24000
	v_cvt_pk_fp8_f32 v52, v54, v55 op_sel:[0,0,1]
	v_med3_f32 v46, v46, s51, v187
	v_med3_f32 v47, v47, s51, v187
	v_pk_fma_f32 v[38:39], v[38:39], s[82:83], v[66:67] op_sel_hi:[1,0,1]
	v_cvt_pk_fp8_f32 v20, v22, v23 op_sel:[0,0,1]
	v_med3_f32 v14, v14, s51, v187
	v_med3_f32 v15, v15, s51, v187
	v_pk_fma_f32 v[6:7], v[6:7], s[82:83], v[66:67] op_sel_hi:[1,0,1]
	v_pk_fma_f32 v[2:3], v[2:3], s[82:83], v[70:71] op_sel_hi:[1,0,1]
	v_lshl_add_u64 v[88:89], v[120:121], 0, s[16:17]
	s_mov_b64 s[16:17], 0x28000
	v_cvt_pk_fp8_f32 v44, v46, v47 op_sel:[0,0,1]
	v_med3_f32 v38, v38, s51, v187
	v_med3_f32 v39, v39, s51, v187
	v_cvt_pk_fp8_f32 v12, v14, v15 op_sel:[0,0,1]
	v_med3_f32 v6, v6, s51, v187
	v_med3_f32 v7, v7, s51, v187
	v_med3_f32 v0, v2, s51, v187
	v_med3_f32 v1, v3, s51, v187
	v_lshl_add_u64 v[80:81], v[120:121], 0, s[16:17]
	s_mov_b64 s[16:17], 0x2c000
	v_cvt_pk_fp8_f32 v36, v38, v39 op_sel:[0,0,1]
	v_cvt_pk_fp8_f32 v4, v6, v7 op_sel:[0,0,1]
	v_cvt_pk_fp8_f32 v5, v0, v1 op_sel:[0,0,1]
	s_andn2_b64 vcc, exec, s[12:13]
	s_mov_b64 s[12:13], -1
	v_lshl_add_u64 v[112:113], v[120:121], 0, s[60:61]
	v_lshl_add_u64 v[72:73], v[120:121], 0, s[16:17]
	v_mov_b32_e32 v192, v60
	v_mov_b32_e32 v193, v61
	v_mov_b32_e32 v194, v52
	v_mov_b32_e32 v195, v53
	v_mov_b32_e32 v196, v44
	v_mov_b32_e32 v197, v45
	v_mov_b32_e32 v198, v36
	v_mov_b32_e32 v199, v37
	v_mov_b32_e32 v200, v28
	v_mov_b32_e32 v201, v29
	v_mov_b32_e32 v202, v20
	v_mov_b32_e32 v203, v21
	v_mov_b32_e32 v204, v12
	v_mov_b32_e32 v205, v13
	v_mov_b32_e32 v206, v4
	v_mov_b32_e32 v207, v5
	v_permlane16_swap_b32_e32 v192, v194
	v_permlane16_swap_b32_e32 v193, v195
	v_permlane16_swap_b32_e32 v196, v198
	v_permlane16_swap_b32_e32 v197, v199
	v_permlane16_swap_b32_e32 v200, v202
	v_permlane16_swap_b32_e32 v201, v203
	v_lshl_add_u64 v[232:233], v[120:121], 0, v[152:153]
	v_lshl_add_u64 v[234:235], v[112:113], 0, v[152:153]
	v_permlane16_swap_b32_e32 v204, v206
	v_permlane16_swap_b32_e32 v205, v207
	v_lshl_add_u64 v[236:237], v[96:97], 0, v[152:153]
	v_lshl_add_u64 v[238:239], v[80:81], 0, v[152:153]
	global_store_dwordx4 v[232:233], v[192:195], off offset:128
	global_store_dwordx4 v[234:235], v[196:199], off offset:128
	global_store_dwordx4 v[236:237], v[200:203], off offset:128
	global_store_dwordx4 v[238:239], v[204:207], off offset:128
	s_cbranch_vccnz .LBB0_853
	s_andn2_b64 vcc, exec, s[0:1]
	s_cbranch_vccnz .LBB0_852
	s_barrier
	s_branch .LBB0_852
